# baseline (speedup 1.0000x reference)
_ZN12_GLOBAL__N_113search_kernelEPKfS1_PhPf:
	s_load_dwordx2 s[8:9], s[0:1], 0x0
	s_load_dwordx2 s[4:5], s[0:1], 0x10
	s_movk_i32 s3, 0x90
	v_readfirstlane_b32 s10, v0
	v_cmp_gt_u32_e32 vcc, s3, v0
	s_and_saveexec_b64 s[6:7], vcc
	v_mov_b32_e32 v2, -1
	v_lshlrev_b32_e32 v1, 3, v0
	v_mov_b32_e32 v3, v2
	ds_write_b64 v1, v[2:3] offset:16384
	s_or_b64 exec, exec, s[6:7]
	s_waitcnt lgkmcnt(0)
	s_add_u32 s6, s4, 0x240000
	s_addc_u32 s7, s5, 0
	s_lshl_b32 s11, s2, 1
	s_and_b32 s14, s11, 14
	s_ashr_i32 s11, s2, 7
	s_lshr_b32 s15, s10, 6
	s_add_i32 s14, s14, s11
	s_bfe_u32 s2, s2, 0x40003
	s_mul_i32 s11, s15, 24
	v_mul_u32_u24_e32 v2, 0x71d, v0
	v_mul_u32_u24_e32 v4, 0x195, v0
	s_min_u32 s18, s11, 0xa5
	s_mul_i32 s11, s14, 3
	s_mul_i32 s12, s2, 9
	s_mov_b32 s13, 0
	v_lshrrev_b32_e32 v3, 16, v2
	s_movk_i32 s19, 0xffdc
	v_lshrrev_b32_e32 v5, 17, v4
	v_mad_i32_i24 v2, v3, s19, v0
	v_mad_i32_i24 v4, v5, -9, v3
	v_add_u32_e32 v3, s11, v5
	v_mov_b64_e32 v[6:7], s[12:13]
	v_mad_i64_i32 v[8:9], s[16:17], v3, s3, v[6:7]
	v_ashrrev_i32_e32 v5, 31, v4
	v_lshl_add_u64 v[4:5], v[8:9], 0, v[4:5]
	s_movk_i32 s13, 0x240
	v_mov_b64_e32 v[8:9], s[8:9]
	v_mad_u64_u32 v[10:11], s[8:9], v4, s13, v[8:9]
	v_min_u32_e32 v4, 0x1cb, v0
	v_or_b32_e32 v4, 0x200, v4
	v_mad_i32_i24 v11, v5, s13, v11
	v_mul_u32_u24_e32 v5, 0x71d, v4
	v_ashrrev_i32_e32 v3, 31, v2
	v_lshrrev_b32_e32 v5, 16, v5
	v_lshl_add_u64 v[2:3], v[2:3], 4, v[10:11]
	v_mad_i32_i24 v10, v5, s19, v4
	v_mul_u32_u24_e32 v4, 0x653, v4
	v_lshrrev_b32_e32 v11, 19, v4
	v_mad_i32_i24 v4, v11, -9, v5
	v_add_u32_e32 v5, s11, v11
	v_mad_i64_i32 v[6:7], s[8:9], v5, s3, v[6:7]
	v_ashrrev_i32_e32 v5, 31, v4
	v_lshl_add_u64 v[4:5], v[6:7], 0, v[4:5]
	v_mad_u64_u32 v[12:13], s[8:9], v4, s13, v[8:9]
	s_mul_i32 s8, s14, 0x90
	s_barrier
	global_load_dwordx4 v[6:9], v[2:3], off
	s_add_i32 s3, s8, s12
	v_and_b32_e32 v210, 15, v0
	v_lshlrev_b32_e32 v252, 3, v210
	v_bfe_u32 v253, v0, 4, 2
	s_lshl_b32 s11, s3, 6
	v_and_b32_e32 v2, 48, v0
	s_mul_i32 s9, s14, 0xbd
	v_or3_b32 v2, s11, v2, v210
	s_add_i32 s18, s18, s9
	v_and_b32_e32 v1, 63, v0
	v_ashrrev_i32_e32 v3, 31, v2
	s_lshl_b32 s3, s18, 6
	v_mad_i32_i24 v13, v5, s13, v13
	v_lshl_add_u64 v[14:15], v[2:3], 4, s[4:5]
	v_or_b32_e32 v2, s3, v1
	v_ashrrev_i32_e32 v11, 31, v10
	v_ashrrev_i32_e32 v3, 31, v2
	v_lshl_add_u64 v[10:11], v[10:11], 4, v[12:13]
	v_lshl_add_u64 v[16:17], v[2:3], 4, s[6:7]
	global_load_dwordx4 v[2:5], v[14:15], off
	global_load_dwordx4 v[58:61], v[16:17], off
	s_add_i32 s12, s3, 64
	global_load_dwordx4 v[10:13], v[10:11], off
	v_or_b32_e32 v14, s12, v1
	v_ashrrev_i32_e32 v15, 31, v14
	v_lshl_add_u64 v[14:15], v[14:15], 4, s[6:7]
	s_add_i32 s12, s3, 0x80
	global_load_dwordx4 v[54:57], v[14:15], off
	v_or_b32_e32 v14, s12, v1
	v_ashrrev_i32_e32 v15, 31, v14
	v_lshl_add_u64 v[14:15], v[14:15], 4, s[6:7]
	s_add_i32 s12, s3, 0xc0
	global_load_dwordx4 v[98:101], v[14:15], off
	v_or_b32_e32 v14, s12, v1
	v_ashrrev_i32_e32 v15, 31, v14
	v_lshl_add_u64 v[14:15], v[14:15], 4, s[6:7]
	s_add_i32 s12, s11, 64
	global_load_dwordx4 v[82:85], v[14:15], off
	v_or_b32_e32 v14, s12, v1
	v_ashrrev_i32_e32 v15, 31, v14
	v_lshl_add_u64 v[14:15], v[14:15], 4, s[4:5]
	s_add_i32 s12, s11, 0x80
	global_load_dwordx4 v[34:37], v[14:15], off
	v_or_b32_e32 v14, s12, v1
	s_add_i32 s12, s11, 0xc0
	v_or_b32_e32 v16, s12, v1
	s_add_i32 s12, s11, 0x100
	v_or_b32_e32 v18, s12, v1
	s_add_i32 s12, s11, 0x140
	v_ashrrev_i32_e32 v15, 31, v14
	v_ashrrev_i32_e32 v17, 31, v16
	v_or_b32_e32 v20, s12, v1
	v_lshl_add_u64 v[14:15], v[14:15], 4, s[4:5]
	v_lshl_add_u64 v[16:17], v[16:17], 4, s[4:5]
	v_ashrrev_i32_e32 v21, 31, v20
	s_add_i32 s12, s11, 0x180
	global_load_dwordx4 v[30:33], v[14:15], off
	global_load_dwordx4 v[26:29], v[16:17], off
	v_lshl_add_u64 v[14:15], v[20:21], 4, s[4:5]
	v_or_b32_e32 v20, s12, v1
	v_ashrrev_i32_e32 v21, 31, v20
	s_add_i32 s12, s11, 0x1c0
	v_lshl_add_u64 v[38:39], v[20:21], 4, s[4:5]
	v_or_b32_e32 v20, s12, v1
	v_ashrrev_i32_e32 v21, 31, v20
	s_addk_i32 s11, 0x200
	v_lshl_add_u64 v[40:41], v[20:21], 4, s[4:5]
	v_or_b32_e32 v20, s11, v1
	v_ashrrev_i32_e32 v21, 31, v20
	s_add_i32 s11, s3, 0x100
	v_lshl_add_u64 v[42:43], v[20:21], 4, s[4:5]
	v_or_b32_e32 v20, s11, v1
	s_add_i32 s11, s3, 0x140
	v_or_b32_e32 v16, s11, v1
	v_ashrrev_i32_e32 v17, 31, v16
	s_add_i32 s11, s3, 0x180
	v_lshl_add_u64 v[46:47], v[16:17], 4, s[6:7]
	v_or_b32_e32 v16, s11, v1
	v_ashrrev_i32_e32 v17, 31, v16
	s_add_i32 s11, s3, 0x1c0
	v_lshl_add_u64 v[48:49], v[16:17], 4, s[6:7]
	v_or_b32_e32 v16, s11, v1
	v_ashrrev_i32_e32 v17, 31, v16
	s_add_i32 s11, s3, 0x200
	v_lshl_add_u64 v[50:51], v[16:17], 4, s[6:7]
	v_or_b32_e32 v16, s11, v1
	v_ashrrev_i32_e32 v17, 31, v16
	s_add_i32 s11, s3, 0x240
	v_lshl_add_u64 v[52:53], v[16:17], 4, s[6:7]
	v_or_b32_e32 v16, s11, v1
	v_ashrrev_i32_e32 v17, 31, v16
	s_add_i32 s11, s3, 0x280
	v_ashrrev_i32_e32 v19, 31, v18
	v_ashrrev_i32_e32 v21, 31, v20
	v_lshl_add_u64 v[66:67], v[16:17], 4, s[6:7]
	v_or_b32_e32 v16, s11, v1
	v_lshl_add_u64 v[18:19], v[18:19], 4, s[4:5]
	v_lshl_add_u64 v[44:45], v[20:21], 4, s[6:7]
	v_ashrrev_i32_e32 v17, 31, v16
	s_add_i32 s11, s3, 0x2c0
	global_load_dwordx4 v[22:25], v[18:19], off
	v_lshl_add_u64 v[86:87], v[16:17], 4, s[6:7]
	v_or_b32_e32 v16, s11, v1
	s_add_i32 s11, s3, 0x300
	global_load_dwordx4 v[18:21], v[14:15], off
	global_load_dwordx4 v[62:65], v[44:45], off
	v_lshlrev_b32_e32 v14, 4, v0
	s_waitcnt vmcnt(12)
	ds_write_b128 v14, v[6:9]
	v_or_b32_e32 v6, s11, v1
	v_ashrrev_i32_e32 v7, 31, v6
	s_add_i32 s11, s3, 0x340
	v_lshl_add_u64 v[142:143], v[6:7], 4, s[6:7]
	v_or_b32_e32 v6, s11, v1
	v_ashrrev_i32_e32 v7, 31, v6
	s_add_i32 s11, s3, 0x380
	v_lshl_add_u64 v[146:147], v[6:7], 4, s[6:7]
	v_or_b32_e32 v6, s11, v1
	v_ashrrev_i32_e32 v17, 31, v16
	v_ashrrev_i32_e32 v7, 31, v6
	v_lshl_add_u64 v[88:89], v[16:17], 4, s[6:7]
	s_waitcnt vmcnt(9)
	ds_write_b128 v14, v[10:13] offset:8192
	global_load_dwordx4 v[14:17], v[38:39], off
	global_load_dwordx4 v[10:13], v[40:41], off
	v_lshl_add_u64 v[38:39], v[6:7], 4, s[6:7]
	global_load_dwordx4 v[6:9], v[42:43], off
	global_load_dwordx4 v[94:97], v[46:47], off
	global_load_dwordx4 v[78:81], v[48:49], off
	global_load_dwordx4 v[74:77], v[50:51], off
	global_load_dwordx4 v[70:73], v[52:53], off
	s_add_i32 s11, s3, 0x3c0
	v_or_b32_e32 v40, s11, v1
	v_ashrrev_i32_e32 v41, 31, v40
	v_mfma_f32_16x16x32_f16 v[102:105], v[58:61], v[2:5], 0
	v_lshl_add_u64 v[40:41], v[40:41], 4, s[6:7]
	global_load_dwordx4 v[66:69], v[66:67], off
	s_nop 0
	global_load_dwordx4 v[90:93], v[86:87], off
	s_nop 0
	global_load_dwordx4 v[86:89], v[88:89], off
	s_nop 0
	global_load_dwordx4 v[50:53], v[142:143], off
	global_load_dwordx4 v[46:49], v[146:147], off
	global_load_dwordx4 v[42:45], v[38:39], off
	s_nop 0
	global_load_dwordx4 v[38:41], v[40:41], off
	s_waitcnt vmcnt(22)
	v_mfma_f32_16x16x32_f16 v[106:109], v[54:57], v[2:5], 0
	s_mov_b32 s11, 0x7f000000
	v_mov_b32_e32 v159, 0
	v_mov_b32_e32 v171, 0
	s_waitcnt vmcnt(21)
	v_mfma_f32_16x16x32_f16 v[110:113], v[98:101], v[2:5], 0
	v_mov_b32_e32 v173, 0
	v_mov_b32_e32 v197, 0
	v_mov_b32_e32 v195, 0
	s_waitcnt vmcnt(20)
	v_mfma_f32_16x16x32_f16 v[114:117], v[82:85], v[2:5], 0
	v_mov_b32_e32 v199, 0
	v_min_i32_e32 v102, v102, v103
	v_min_i32_e32 v103, v104, v105
	v_min_i32_e32 v104, v106, v107
	v_min_i32_e32 v105, v108, v109
	v_min_i32_e32 v154, v110, v111
	v_min3_i32 v102, v102, v103, v104
	v_min_i32_e32 v155, v112, v113
	v_min_i32_e32 v114, v114, v115
	v_min3_i32 v102, v102, v105, v154
	s_waitcnt vmcnt(19)
	v_mfma_f32_16x16x32_f16 v[118:121], v[58:61], v[34:37], 0
	v_min_i32_e32 v115, v116, v117
	v_min3_i32 v102, v102, v155, v114
	v_min3_i32 v158, v102, v115, s11
	v_mfma_f32_16x16x32_f16 v[122:125], v[54:57], v[34:37], 0
	v_mov_b32_e32 v204, 0
	s_add_i32 s12, s3, 0x400
	v_mov_b32_e32 v205, 0
	v_mfma_f32_16x16x32_f16 v[126:129], v[98:101], v[34:37], 0
	v_mov_b32_e32 v220, 0
	v_mfma_f32_16x16x32_f16 v[130:133], v[82:85], v[34:37], 0
	s_waitcnt vmcnt(18)
	v_mfma_f32_16x16x32_f16 v[134:137], v[58:61], v[30:33], 0
	v_mfma_f32_16x16x32_f16 v[138:141], v[54:57], v[30:33], 0
	v_mfma_f32_16x16x32_f16 v[142:145], v[98:101], v[30:33], 0
	v_mfma_f32_16x16x32_f16 v[146:149], v[82:85], v[30:33], 0
	s_nop 0
	v_min_i32_e32 v102, v118, v119
	v_min_i32_e32 v103, v120, v121
	v_min_i32_e32 v104, v122, v123
	v_min_i32_e32 v105, v124, v125
	v_min_i32_e32 v114, v126, v127
	v_min3_i32 v102, v102, v103, v104
	v_min_i32_e32 v115, v128, v129
	v_min_i32_e32 v116, v130, v131
	v_min3_i32 v102, v102, v105, v114
	v_min_i32_e32 v117, v132, v133
	v_min3_i32 v102, v102, v115, v116
	s_waitcnt vmcnt(17)
	v_mfma_f32_16x16x32_f16 v[150:153], v[58:61], v[26:29], 0
	v_min3_i32 v170, v102, v117, s11
	v_mfma_f32_16x16x32_f16 v[106:109], v[54:57], v[26:29], 0
	v_mfma_f32_16x16x32_f16 v[110:113], v[98:101], v[26:29], 0
	v_mfma_f32_16x16x32_f16 v[154:157], v[82:85], v[26:29], 0
	s_nop 0
	v_min_i32_e32 v114, v134, v135
	v_min_i32_e32 v115, v136, v137
	v_min_i32_e32 v116, v138, v139
	v_min_i32_e32 v117, v140, v141
	v_min_i32_e32 v122, v142, v143
	v_min3_i32 v114, v114, v115, v116
	v_min_i32_e32 v123, v144, v145
	v_min_i32_e32 v124, v146, v147
	v_min3_i32 v114, v114, v117, v122
	v_min_i32_e32 v125, v148, v149
	v_min3_i32 v114, v114, v123, v124
	s_waitcnt vmcnt(16)
	v_mfma_f32_16x16x32_f16 v[160:163], v[58:61], v[22:25], 0
	v_min3_i32 v172, v114, v125, s11
	v_mfma_f32_16x16x32_f16 v[164:167], v[54:57], v[22:25], 0
	v_mfma_f32_16x16x32_f16 v[118:121], v[98:101], v[22:25], 0
	v_mfma_f32_16x16x32_f16 v[128:131], v[82:85], v[22:25], 0
	s_nop 0
	v_min_i32_e32 v110, v110, v111
	s_waitcnt vmcnt(15)
	v_mfma_f32_16x16x32_f16 v[174:177], v[58:61], v[18:21], 0
	v_min_i32_e32 v111, v112, v113
	v_min_i32_e32 v112, v154, v155
	v_min_i32_e32 v113, v156, v157
	s_waitcnt vmcnt(13)
	v_mfma_f32_16x16x32_f16 v[102:105], v[58:61], v[14:17], 0
	s_waitcnt vmcnt(12)
	v_mfma_f32_16x16x32_f16 v[134:137], v[58:61], v[10:13], 0
	s_waitcnt vmcnt(11)
	v_mfma_f32_16x16x32_f16 v[114:117], v[58:61], v[6:9], 0
	v_min_i32_e32 v58, v150, v151
	v_min_i32_e32 v59, v152, v153
	v_min_i32_e32 v60, v106, v107
	v_min_i32_e32 v61, v108, v109
	v_min3_i32 v58, v58, v59, v60
	v_min3_i32 v58, v58, v61, v110
	v_min3_i32 v58, v58, v111, v112
	v_mfma_f32_16x16x32_f16 v[178:181], v[54:57], v[18:21], 0
	v_min3_i32 v196, v58, v113, s11
	v_mfma_f32_16x16x32_f16 v[182:185], v[98:101], v[18:21], 0
	v_mfma_f32_16x16x32_f16 v[186:189], v[82:85], v[18:21], 0
	s_nop 0
	v_min_i32_e32 v110, v160, v161
	v_min_i32_e32 v111, v162, v163
	v_min_i32_e32 v112, v164, v165
	v_mfma_f32_16x16x32_f16 v[142:145], v[54:57], v[14:17], 0
	v_min_i32_e32 v113, v166, v167
	v_min_i32_e32 v118, v118, v119
	v_min_i32_e32 v119, v120, v121
	v_mfma_f32_16x16x32_f16 v[146:149], v[98:101], v[14:17], 0
	v_min_i32_e32 v120, v128, v129
	v_mfma_f32_16x16x32_f16 v[58:61], v[54:57], v[10:13], 0
	v_mfma_f32_16x16x32_f16 v[122:125], v[54:57], v[6:9], 0
	v_mfma_f32_16x16x32_f16 v[54:57], v[98:101], v[10:13], 0
	v_mfma_f32_16x16x32_f16 v[126:129], v[98:101], v[6:9], 0
	v_min3_i32 v99, v110, v111, v112
	v_min3_i32 v99, v99, v113, v118
	v_min_i32_e32 v98, v130, v131
	v_min3_i32 v99, v99, v119, v120
	v_mfma_f32_16x16x32_f16 v[106:109], v[82:85], v[14:17], 0
	v_min3_i32 v194, v99, v98, s11
	v_mfma_f32_16x16x32_f16 v[138:141], v[82:85], v[10:13], 0
	v_min_i32_e32 v98, v182, v183
	v_min_i32_e32 v99, v184, v185
	v_min_i32_e32 v100, v186, v187
	v_mfma_f32_16x16x32_f16 v[130:133], v[82:85], v[6:9], 0
	v_min_i32_e32 v82, v174, v175
	v_min_i32_e32 v83, v176, v177
	v_min_i32_e32 v84, v178, v179
	v_min_i32_e32 v85, v180, v181
	v_min3_i32 v82, v82, v83, v84
	v_min3_i32 v82, v82, v85, v98
	v_min_i32_e32 v101, v188, v189
	v_min3_i32 v82, v82, v99, v100
	v_min3_i32 v198, v82, v101, s11
	v_mfma_f32_16x16x32_f16 v[150:153], v[62:65], v[2:5], 0
	v_min_i32_e32 v82, v102, v103
	v_min_i32_e32 v83, v104, v105
	v_min_i32_e32 v84, v142, v143
	v_min_i32_e32 v85, v144, v145
	v_min_i32_e32 v98, v146, v147
	v_min3_i32 v82, v82, v83, v84
	v_min_i32_e32 v99, v148, v149
	v_min_i32_e32 v100, v106, v107
	v_min3_i32 v82, v82, v85, v98
	v_min_i32_e32 v101, v108, v109
	v_min3_i32 v82, v82, v99, v100
	v_min3_i32 v203, v82, v101, s11
	v_mfma_f32_16x16x32_f16 v[162:165], v[62:65], v[34:37], 0
	v_min_i32_e32 v58, v58, v59
	v_min_i32_e32 v59, v60, v61
	v_min_i32_e32 v54, v54, v55
	v_mfma_f32_16x16x32_f16 v[166:169], v[62:65], v[30:33], 0
	v_min_i32_e32 v55, v56, v57
	v_min_i32_e32 v56, v138, v139
	v_min_i32_e32 v57, v140, v141
	v_mfma_f32_16x16x32_f16 v[154:157], v[62:65], v[26:29], 0
	v_mfma_f32_16x16x32_f16 v[110:113], v[62:65], v[22:25], 0
	v_mfma_f32_16x16x32_f16 v[118:121], v[62:65], v[18:21], 0
	v_mfma_f32_16x16x32_f16 v[102:105], v[62:65], v[14:17], 0
	v_mfma_f32_16x16x32_f16 v[106:109], v[62:65], v[10:13], 0
	v_mfma_f32_16x16x32_f16 v[98:101], v[62:65], v[6:9], 0
	v_min_i32_e32 v62, v134, v135
	v_min_i32_e32 v63, v136, v137
	v_min3_i32 v58, v62, v63, v58
	v_min3_i32 v54, v58, v59, v54
	v_min3_i32 v54, v54, v55, v56
	v_min3_i32 v202, v54, v57, s11
	v_mov_b32_e32 v54, 0
	s_waitcnt vmcnt(10)
	v_mfma_f32_16x16x32_f16 v[174:177], v[94:97], v[2:5], 0
	v_add_u32_e32 v60, v1, v54
	v_add_u32_e32 v54, s12, v60
	s_add_i32 s12, s3, 0x440
	v_add_u32_e32 v56, s12, v60
	s_add_i32 s12, s3, 0x480
	v_add_u32_e32 v58, s12, v60
	s_add_i32 s12, s3, 0x4c0
	v_ashrrev_i32_e32 v55, 31, v54
	v_ashrrev_i32_e32 v57, 31, v56
	v_ashrrev_i32_e32 v59, 31, v58
	v_add_u32_e32 v60, s12, v60
	s_waitcnt vmcnt(9)
	v_mfma_f32_16x16x32_f16 v[134:137], v[78:81], v[2:5], 0
	v_lshl_add_u64 v[54:55], v[54:55], 4, s[6:7]
	v_lshl_add_u64 v[56:57], v[56:57], 4, s[6:7]
	v_lshl_add_u64 v[58:59], v[58:59], 4, s[6:7]
	s_waitcnt vmcnt(8)
	v_mfma_f32_16x16x32_f16 v[178:181], v[74:77], v[2:5], 0
	v_ashrrev_i32_e32 v61, 31, v60
	v_lshl_add_u64 v[138:139], v[60:61], 4, s[6:7]
	global_load_dwordx4 v[82:85], v[54:55], off
	global_load_dwordx4 v[62:65], v[56:57], off
	s_nop 0
	global_load_dwordx4 v[58:61], v[58:59], off
	s_nop 0
	global_load_dwordx4 v[54:57], v[138:139], off
	v_mfma_f32_16x16x32_f16 v[182:185], v[94:97], v[34:37], 0
	v_min_i32_e32 v114, v114, v115
	v_min_i32_e32 v115, v116, v117
	v_min_i32_e32 v116, v122, v123
	v_min_i32_e32 v117, v124, v125
	v_min_i32_e32 v122, v126, v127
	v_min3_i32 v114, v114, v115, v116
	v_min_i32_e32 v123, v128, v129
	v_min_i32_e32 v124, v130, v131
	v_min3_i32 v114, v114, v117, v122
	v_min_i32_e32 v125, v132, v133
	v_min3_i32 v114, v114, v123, v124
	v_mfma_f32_16x16x32_f16 v[206:209], v[78:81], v[34:37], 0
	v_min3_i32 v218, v114, v125, s11
	s_add_i32 s11, s3, 0x500
	s_mov_b32 s12, 0x2aaaaaab
	v_mfma_f32_16x16x32_f16 v[212:215], v[74:77], v[34:37], 0
	s_nop 0
	v_min3_i32 v114, v150, v151, v158
	v_min3_i32 v114, v152, v153, v114
	v_min3_i32 v114, v174, v175, v114
	v_min3_i32 v130, v176, v177, v114
	v_min3_i32 v130, v134, v135, v130
	v_min3_i32 v130, v136, v137, v130
	v_min3_i32 v130, v178, v179, v130
	v_min3_i32 v219, v180, v181, v130
	v_cmp_ge_i32_e32 vcc, v219, v158
	v_mfma_f32_16x16x32_f16 v[224:227], v[94:97], v[30:33], 0
	s_nop 0
	v_cndmask_b32_e32 v221, 1, v159, vcc
	v_mfma_f32_16x16x32_f16 v[228:231], v[78:81], v[30:33], 0
	v_mfma_f32_16x16x32_f16 v[232:235], v[74:77], v[30:33], 0
	s_nop 0
	v_min3_i32 v130, v162, v163, v170
	v_min3_i32 v130, v164, v165, v130
	v_min3_i32 v130, v182, v183, v130
	v_min3_i32 v130, v184, v185, v130
	v_min3_i32 v134, v206, v207, v130
	v_mfma_f32_16x16x32_f16 v[236:239], v[94:97], v[26:29], 0
	v_mfma_f32_16x16x32_f16 v[186:189], v[94:97], v[22:25], 0
	v_mfma_f32_16x16x32_f16 v[146:149], v[94:97], v[18:21], 0
	v_mfma_f32_16x16x32_f16 v[138:141], v[94:97], v[14:17], 0
	v_mfma_f32_16x16x32_f16 v[142:145], v[94:97], v[10:13], 0
	v_mfma_f32_16x16x32_f16 v[126:129], v[94:97], v[6:9], 0
	v_mfma_f32_16x16x32_f16 v[94:97], v[78:81], v[26:29], 0
	v_mfma_f32_16x16x32_f16 v[190:193], v[78:81], v[22:25], 0
	v_mfma_f32_16x16x32_f16 v[174:177], v[78:81], v[18:21], 0
	v_mfma_f32_16x16x32_f16 v[158:161], v[78:81], v[14:17], 0
	v_mfma_f32_16x16x32_f16 v[162:165], v[78:81], v[10:13], 0
	v_mfma_f32_16x16x32_f16 v[130:133], v[78:81], v[6:9], 0
	v_min3_i32 v78, v208, v209, v134
	v_min3_i32 v78, v212, v213, v78
	v_min3_i32 v217, v214, v215, v78
	v_cmp_ge_i32_e32 vcc, v217, v170
	v_mfma_f32_16x16x32_f16 v[122:125], v[74:77], v[26:29], 0
	s_nop 0
	v_cndmask_b32_e32 v222, 1, v171, vcc
	v_mfma_f32_16x16x32_f16 v[114:117], v[74:77], v[22:25], 0
	v_min3_i32 v78, v166, v167, v172
	v_min3_i32 v78, v168, v169, v78
	v_min3_i32 v78, v224, v225, v78
	v_min3_i32 v134, v226, v227, v78
	v_min3_i32 v134, v228, v229, v134
	v_min3_i32 v134, v230, v231, v134
	v_min3_i32 v134, v232, v233, v134
	v_min3_i32 v211, v234, v235, v134
	v_cmp_ge_i32_e32 vcc, v211, v172
	v_mfma_f32_16x16x32_f16 v[182:185], v[74:77], v[18:21], 0
	s_nop 0
	v_cndmask_b32_e32 v213, 1, v173, vcc
	v_mfma_f32_16x16x32_f16 v[178:181], v[74:77], v[14:17], 0
	v_mfma_f32_16x16x32_f16 v[78:81], v[74:77], v[10:13], 0
	v_mfma_f32_16x16x32_f16 v[150:153], v[74:77], v[6:9], 0
	v_min3_i32 v74, v154, v155, v196
	v_min3_i32 v74, v156, v157, v74
	v_min3_i32 v74, v236, v237, v74
	v_min3_i32 v74, v238, v239, v74
	v_min3_i32 v74, v94, v95, v74
	v_min3_i32 v74, v96, v97, v74
	v_min3_i32 v74, v122, v123, v74
	v_min3_i32 v212, v124, v125, v74
	v_cmp_ge_i32_e32 vcc, v212, v196
	s_waitcnt vmcnt(11)
	v_mfma_f32_16x16x32_f16 v[166:169], v[70:73], v[2:5], 0
	v_cndmask_b32_e32 v214, 1, v197, vcc
	v_mfma_f32_16x16x32_f16 v[170:173], v[70:73], v[34:37], 0
	v_min3_i32 v74, v110, v111, v194
	v_min3_i32 v74, v112, v113, v74
	v_min3_i32 v74, v186, v187, v74
	v_min3_i32 v74, v188, v189, v74
	v_min3_i32 v74, v190, v191, v74
	v_min3_i32 v74, v192, v193, v74
	v_min3_i32 v74, v114, v115, v74
	v_min3_i32 v215, v116, v117, v74
	v_cmp_ge_i32_e32 vcc, v215, v194
	v_mfma_f32_16x16x32_f16 v[154:157], v[70:73], v[30:33], 0
	s_nop 0
	v_cndmask_b32_e32 v216, 1, v195, vcc
	v_mfma_f32_16x16x32_f16 v[134:137], v[70:73], v[26:29], 0
	v_min3_i32 v74, v118, v119, v198
	v_min3_i32 v74, v120, v121, v74
	v_mfma_f32_16x16x32_f16 v[122:125], v[70:73], v[22:25], 0
	v_mfma_f32_16x16x32_f16 v[94:97], v[70:73], v[18:21], 0
	v_mfma_f32_16x16x32_f16 v[110:113], v[70:73], v[14:17], 0
	v_mfma_f32_16x16x32_f16 v[114:117], v[70:73], v[10:13], 0
	v_mfma_f32_16x16x32_f16 v[118:121], v[70:73], v[6:9], 0
	v_min3_i32 v70, v146, v147, v74
	v_min3_i32 v70, v148, v149, v70
	v_min3_i32 v70, v174, v175, v70
	v_min3_i32 v70, v176, v177, v70
	v_min3_i32 v70, v182, v183, v70
	v_min3_i32 v223, v184, v185, v70
	v_cmp_ge_i32_e32 vcc, v223, v198
	s_waitcnt vmcnt(10)
	v_mfma_f32_16x16x32_f16 v[186:189], v[66:69], v[2:5], 0
	v_cndmask_b32_e32 v244, 1, v199, vcc
	v_mfma_f32_16x16x32_f16 v[190:193], v[66:69], v[34:37], 0
	v_min3_i32 v70, v102, v103, v203
	v_min3_i32 v70, v104, v105, v70
	v_min3_i32 v70, v138, v139, v70
	v_min3_i32 v70, v140, v141, v70
	v_min3_i32 v70, v158, v159, v70
	v_min3_i32 v70, v160, v161, v70
	v_min3_i32 v70, v178, v179, v70
	v_min3_i32 v245, v180, v181, v70
	v_cmp_ge_i32_e32 vcc, v245, v203
	v_mfma_f32_16x16x32_f16 v[224:227], v[66:69], v[30:33], 0
	s_nop 0
	v_cndmask_b32_e32 v246, 1, v204, vcc
	v_mfma_f32_16x16x32_f16 v[198:201], v[66:69], v[26:29], 0
	v_min3_i32 v70, v106, v107, v202
	v_min3_i32 v70, v108, v109, v70
	v_min3_i32 v70, v142, v143, v70
	v_mfma_f32_16x16x32_f16 v[158:161], v[66:69], v[22:25], 0
	v_min3_i32 v70, v144, v145, v70
	v_min3_i32 v70, v162, v163, v70
	v_min3_i32 v70, v164, v165, v70
	v_mfma_f32_16x16x32_f16 v[146:149], v[66:69], v[18:21], 0
	v_min3_i32 v70, v78, v79, v70
	v_min3_i32 v247, v80, v81, v70
	v_cmp_ge_i32_e32 vcc, v247, v202
	v_mfma_f32_16x16x32_f16 v[138:141], v[66:69], v[14:17], 0
	s_nop 0
	v_cndmask_b32_e32 v248, 1, v205, vcc
	v_mfma_f32_16x16x32_f16 v[106:109], v[66:69], v[10:13], 0
	v_mfma_f32_16x16x32_f16 v[102:105], v[66:69], v[6:9], 0
	v_mov_b32_e32 v66, 0
	s_nop 0
	v_add_u32_e32 v72, v1, v66
	v_add_u32_e32 v66, s11, v72
	s_add_i32 s11, s3, 0x540
	v_add_u32_e32 v68, s11, v72
	s_add_i32 s11, s3, 0x580
	v_add_u32_e32 v70, s11, v72
	s_addk_i32 s3, 0x5c0
	v_ashrrev_i32_e32 v67, 31, v66
	v_ashrrev_i32_e32 v69, 31, v68
	v_ashrrev_i32_e32 v71, 31, v70
	v_add_u32_e32 v72, s3, v72
	s_waitcnt vmcnt(9)
	v_mfma_f32_16x16x32_f16 v[178:181], v[90:93], v[2:5], 0
	v_lshl_add_u64 v[66:67], v[66:67], 4, s[6:7]
	v_lshl_add_u64 v[68:69], v[68:69], 4, s[6:7]
	v_lshl_add_u64 v[70:71], v[70:71], 4, s[6:7]
	s_waitcnt vmcnt(8)
	v_mfma_f32_16x16x32_f16 v[194:197], v[86:89], v[2:5], 0
	v_ashrrev_i32_e32 v73, 31, v72
	v_lshl_add_u64 v[142:143], v[72:73], 4, s[6:7]
	global_load_dwordx4 v[78:81], v[66:67], off
	global_load_dwordx4 v[74:77], v[68:69], off
	s_nop 0
	global_load_dwordx4 v[70:73], v[70:71], off
	s_nop 0
	global_load_dwordx4 v[66:69], v[142:143], off
	v_mfma_f32_16x16x32_f16 v[228:231], v[90:93], v[34:37], 0
	v_min3_i32 v98, v98, v99, v218
	v_min3_i32 v98, v100, v101, v98
	v_min3_i32 v98, v126, v127, v98
	v_min3_i32 v98, v128, v129, v98
	v_min3_i32 v98, v130, v131, v98
	v_min3_i32 v98, v132, v133, v98
	v_min3_i32 v98, v150, v151, v98
	v_min3_i32 v249, v152, v153, v98
	v_cmp_ge_i32_e32 vcc, v249, v218
	v_mfma_f32_16x16x32_f16 v[232:235], v[86:89], v[34:37], 0
	s_mul_i32 s3, s15, 6
	v_cndmask_b32_e32 v218, 1, v220, vcc
	v_mfma_f32_16x16x32_f16 v[236:239], v[90:93], v[30:33], 0
	v_min3_i32 v98, v166, v167, v219
	s_mul_i32 s11, s2, 0x90
	v_mfma_f32_16x16x32_f16 v[206:209], v[90:93], v[26:29], 0
	v_mfma_f32_16x16x32_f16 v[182:185], v[90:93], v[22:25], 0
	v_mfma_f32_16x16x32_f16 v[174:177], v[90:93], v[18:21], 0
	v_mfma_f32_16x16x32_f16 v[162:165], v[90:93], v[14:17], 0
	v_mfma_f32_16x16x32_f16 v[142:145], v[90:93], v[10:13], 0
	v_mfma_f32_16x16x32_f16 v[126:129], v[90:93], v[6:9], 0
	v_min3_i32 v90, v168, v169, v98
	v_min3_i32 v90, v186, v187, v90
	v_min3_i32 v98, v188, v189, v90
	v_min3_i32 v98, v178, v179, v98
	v_min3_i32 v98, v180, v181, v98
	v_min3_i32 v98, v194, v195, v98
	v_min3_i32 v220, v196, v197, v98
	v_cmp_ge_i32_e32 vcc, v220, v219
	v_mfma_f32_16x16x32_f16 v[240:243], v[86:89], v[30:33], 0
	s_nop 0
	v_cndmask_b32_e32 v219, 2, v221, vcc
	v_mfma_f32_16x16x32_f16 v[90:93], v[86:89], v[26:29], 0
	v_min3_i32 v98, v170, v171, v217
	v_min3_i32 v98, v172, v173, v98
	v_min3_i32 v98, v190, v191, v98
	v_min3_i32 v98, v192, v193, v98
	v_min3_i32 v98, v228, v229, v98
	v_min3_i32 v98, v230, v231, v98
	v_min3_i32 v98, v232, v233, v98
	v_min3_i32 v221, v234, v235, v98
	v_cmp_ge_i32_e32 vcc, v221, v217
	v_mfma_f32_16x16x32_f16 v[202:205], v[86:89], v[22:25], 0
	s_nop 0
	v_cndmask_b32_e32 v217, 2, v222, vcc
	v_mfma_f32_16x16x32_f16 v[194:197], v[86:89], v[18:21], 0
	v_mfma_f32_16x16x32_f16 v[186:189], v[86:89], v[14:17], 0
	v_mfma_f32_16x16x32_f16 v[166:169], v[86:89], v[10:13], 0
	v_mfma_f32_16x16x32_f16 v[150:153], v[86:89], v[6:9], 0
	v_min3_i32 v86, v154, v155, v211
	v_min3_i32 v86, v156, v157, v86
	v_min3_i32 v86, v224, v225, v86
	v_min3_i32 v86, v226, v227, v86
	v_min3_i32 v86, v236, v237, v86
	v_min3_i32 v86, v238, v239, v86
	v_min3_i32 v86, v240, v241, v86
	v_min3_i32 v222, v242, v243, v86
	v_cmp_ge_i32_e32 vcc, v222, v211
	s_waitcnt vmcnt(11)
	v_mfma_f32_16x16x32_f16 v[170:173], v[50:53], v[2:5], 0
	v_cndmask_b32_e32 v211, 2, v213, vcc
	v_mfma_f32_16x16x32_f16 v[154:157], v[50:53], v[34:37], 0
	v_min3_i32 v86, v134, v135, v212
	v_min3_i32 v86, v136, v137, v86
	v_min3_i32 v86, v198, v199, v86
	v_min3_i32 v86, v200, v201, v86
	v_min3_i32 v86, v206, v207, v86
	v_min3_i32 v86, v208, v209, v86
	v_min3_i32 v86, v90, v91, v86
	v_min3_i32 v198, v92, v93, v86
	v_cmp_ge_i32_e32 vcc, v198, v212
	s_waitcnt vmcnt(10)
	v_mfma_f32_16x16x32_f16 v[134:137], v[46:49], v[2:5], 0
	v_cndmask_b32_e32 v199, 2, v214, vcc
	v_mfma_f32_16x16x32_f16 v[178:181], v[50:53], v[30:33], 0
	v_min3_i32 v122, v122, v123, v215
	v_min3_i32 v122, v124, v125, v122
	v_min3_i32 v122, v158, v159, v122
	v_min3_i32 v122, v160, v161, v122
	v_min3_i32 v122, v182, v183, v122
	v_min3_i32 v122, v184, v185, v122
	v_min3_i32 v122, v202, v203, v122
	v_min3_i32 v200, v204, v205, v122
	v_cmp_ge_i32_e32 vcc, v200, v215
	s_waitcnt vmcnt(9)
	v_mfma_f32_16x16x32_f16 v[158:161], v[42:45], v[2:5], 0
	v_cndmask_b32_e32 v201, 2, v216, vcc
	s_waitcnt vmcnt(8)
	v_mfma_f32_16x16x32_f16 v[182:185], v[38:41], v[2:5], 0
	v_min3_i32 v94, v94, v95, v223
	v_min3_i32 v94, v96, v97, v94
	v_min3_i32 v94, v146, v147, v94
	v_min3_i32 v94, v148, v149, v94
	v_min3_i32 v94, v174, v175, v94
	v_min3_i32 v94, v176, v177, v94
	v_min3_i32 v94, v194, v195, v94
	v_min3_i32 v202, v196, v197, v94
	v_cmp_ge_i32_e32 vcc, v202, v223
	v_mfma_f32_16x16x32_f16 v[146:149], v[46:49], v[34:37], 0
	s_nop 0
	v_cndmask_b32_e32 v203, 2, v244, vcc
	v_mfma_f32_16x16x32_f16 v[174:177], v[42:45], v[34:37], 0
	v_min3_i32 v94, v110, v111, v245
	v_min3_i32 v94, v112, v113, v94
	v_min3_i32 v94, v138, v139, v94
	v_min3_i32 v94, v140, v141, v94
	v_min3_i32 v94, v162, v163, v94
	v_min3_i32 v94, v164, v165, v94
	v_min3_i32 v94, v186, v187, v94
	v_min3_i32 v204, v188, v189, v94
	v_cmp_ge_i32_e32 vcc, v204, v245
	v_mfma_f32_16x16x32_f16 v[194:197], v[38:41], v[34:37], 0
	s_nop 0
	v_cndmask_b32_e32 v205, 2, v246, vcc
	v_mfma_f32_16x16x32_f16 v[110:113], v[46:49], v[30:33], 0
	v_min3_i32 v94, v114, v115, v247
	v_min3_i32 v94, v116, v117, v94
	v_min3_i32 v94, v106, v107, v94
	v_min3_i32 v94, v108, v109, v94
	v_min3_i32 v94, v142, v143, v94
	v_min3_i32 v94, v144, v145, v94
	v_min3_i32 v94, v166, v167, v94
	v_min3_i32 v206, v168, v169, v94
	v_cmp_ge_i32_e32 vcc, v206, v247
	v_mfma_f32_16x16x32_f16 v[190:193], v[50:53], v[26:29], 0
	s_nop 0
	v_cndmask_b32_e32 v207, 2, v248, vcc
	v_mfma_f32_16x16x32_f16 v[138:141], v[46:49], v[26:29], 0
	v_min3_i32 v114, v118, v119, v249
	v_min3_i32 v114, v120, v121, v114
	v_min3_i32 v102, v102, v103, v114
	v_min3_i32 v102, v104, v105, v102
	v_min3_i32 v102, v126, v127, v102
	v_min3_i32 v102, v128, v129, v102
	v_min3_i32 v102, v150, v151, v102
	v_min3_i32 v208, v152, v153, v102
	v_cmp_ge_i32_e32 vcc, v208, v249
	v_mfma_f32_16x16x32_f16 v[118:121], v[42:45], v[30:33], 0
	s_nop 0
	v_cndmask_b32_e32 v209, 2, v218, vcc
	v_mfma_f32_16x16x32_f16 v[126:129], v[38:41], v[30:33], 0
	v_min3_i32 v102, v170, v171, v220
	v_min3_i32 v102, v172, v173, v102
	v_min3_i32 v102, v134, v135, v102
	v_min3_i32 v102, v136, v137, v102
	v_min3_i32 v102, v158, v159, v102
	v_min3_i32 v102, v160, v161, v102
	v_min3_i32 v102, v182, v183, v102
	v_min3_i32 v182, v184, v185, v102
	v_cmp_ge_i32_e32 vcc, v182, v220
	v_mfma_f32_16x16x32_f16 v[142:145], v[42:45], v[26:29], 0
	s_nop 0
	v_cndmask_b32_e32 v183, 3, v219, vcc
	v_mfma_f32_16x16x32_f16 v[150:153], v[38:41], v[26:29], 0
	v_min3_i32 v102, v154, v155, v221
	v_min3_i32 v102, v156, v157, v102
	v_min3_i32 v102, v146, v147, v102
	v_min3_i32 v134, v148, v149, v102
	v_min3_i32 v134, v174, v175, v134
	v_min3_i32 v134, v176, v177, v134
	v_min3_i32 v134, v194, v195, v134
	v_min3_i32 v174, v196, v197, v134
	v_cmp_ge_i32_e32 vcc, v174, v221
	v_mfma_f32_16x16x32_f16 v[130:133], v[50:53], v[22:25], 0
	s_nop 0
	v_cndmask_b32_e32 v175, 3, v217, vcc
	v_mfma_f32_16x16x32_f16 v[186:189], v[46:49], v[22:25], 0
	v_min3_i32 v134, v178, v179, v222
	v_min3_i32 v134, v180, v181, v134
	v_min3_i32 v110, v110, v111, v134
	v_min3_i32 v110, v112, v113, v110
	v_min3_i32 v110, v118, v119, v110
	v_min3_i32 v110, v120, v121, v110
	v_min3_i32 v110, v126, v127, v110
	v_min3_i32 v176, v128, v129, v110
	v_cmp_ge_i32_e32 vcc, v176, v222
	v_mfma_f32_16x16x32_f16 v[166:169], v[42:45], v[22:25], 0
	s_nop 0
	v_cndmask_b32_e32 v177, 3, v211, vcc
	v_mfma_f32_16x16x32_f16 v[170:173], v[38:41], v[22:25], 0
	s_nop 0
	v_min3_i32 v118, v190, v191, v198
	v_mfma_f32_16x16x32_f16 v[162:165], v[38:41], v[18:21], 0
	v_mfma_f32_16x16x32_f16 v[146:149], v[38:41], v[14:17], 0
	v_mfma_f32_16x16x32_f16 v[126:129], v[38:41], v[10:13], 0
	v_mfma_f32_16x16x32_f16 v[110:113], v[38:41], v[6:9], 0
	v_min3_i32 v38, v192, v193, v118
	v_min3_i32 v38, v138, v139, v38
	v_min3_i32 v38, v140, v141, v38
	v_min3_i32 v38, v142, v143, v38
	v_min3_i32 v38, v144, v145, v38
	v_min3_i32 v38, v150, v151, v38
	v_min3_i32 v178, v152, v153, v38
	v_cmp_ge_i32_e32 vcc, v178, v198
	v_mfma_f32_16x16x32_f16 v[98:101], v[50:53], v[18:21], 0
	s_nop 0
	v_cndmask_b32_e32 v179, 3, v199, vcc
	v_mfma_f32_16x16x32_f16 v[122:125], v[46:49], v[18:21], 0
	v_mfma_f32_16x16x32_f16 v[158:161], v[42:45], v[18:21], 0
	s_nop 0
	v_min3_i32 v38, v130, v131, v200
	v_min3_i32 v38, v132, v133, v38
	v_min3_i32 v38, v186, v187, v38
	v_min3_i32 v38, v188, v189, v38
	v_min3_i32 v38, v166, v167, v38
	v_min3_i32 v38, v168, v169, v38
	v_min3_i32 v38, v170, v171, v38
	v_min3_i32 v166, v172, v173, v38
	v_cmp_ge_i32_e32 vcc, v166, v200
	v_mfma_f32_16x16x32_f16 v[86:89], v[50:53], v[14:17], 0
	s_nop 0
	v_cndmask_b32_e32 v167, 3, v201, vcc
	v_mfma_f32_16x16x32_f16 v[106:109], v[46:49], v[14:17], 0
	v_mfma_f32_16x16x32_f16 v[114:117], v[42:45], v[14:17], 0
	s_nop 0
	v_min3_i32 v38, v98, v99, v202
	v_min3_i32 v38, v100, v101, v38
	v_min3_i32 v38, v122, v123, v38
	v_min3_i32 v38, v124, v125, v38
	v_min3_i32 v38, v158, v159, v38
	v_min3_i32 v38, v160, v161, v38
	v_min3_i32 v122, v162, v163, v38
	v_min3_i32 v158, v164, v165, v122
	v_cmp_ge_i32_e32 vcc, v158, v202
	v_mfma_f32_16x16x32_f16 v[90:93], v[50:53], v[10:13], 0
	s_nop 0
	v_cndmask_b32_e32 v159, 3, v203, vcc
	v_mfma_f32_16x16x32_f16 v[94:97], v[46:49], v[10:13], 0
	v_mfma_f32_16x16x32_f16 v[102:105], v[42:45], v[10:13], 0
	s_nop 0
	v_min3_i32 v86, v86, v87, v204
	v_min3_i32 v122, v88, v89, v86
	v_min3_i32 v106, v106, v107, v122
	v_min3_i32 v106, v108, v109, v106
	v_min3_i32 v114, v114, v115, v106
	v_min3_i32 v114, v116, v117, v114
	v_min3_i32 v114, v146, v147, v114
	v_min3_i32 v146, v148, v149, v114
	v_cmp_ge_i32_e32 vcc, v146, v204
	v_mfma_f32_16x16x32_f16 v[50:53], v[50:53], v[6:9], 0
	s_nop 0
	v_cndmask_b32_e32 v147, 3, v205, vcc
	v_mfma_f32_16x16x32_f16 v[46:49], v[46:49], v[6:9], 0
	v_mfma_f32_16x16x32_f16 v[42:45], v[42:45], v[6:9], 0
	s_nop 0
	v_min3_i32 v90, v90, v91, v206
	v_min3_i32 v90, v92, v93, v90
	v_min3_i32 v90, v94, v95, v90
	v_min3_i32 v94, v96, v97, v90
	v_min3_i32 v94, v102, v103, v94
	v_min3_i32 v94, v104, v105, v94
	v_min3_i32 v102, v126, v127, v94
	v_min3_i32 v148, v128, v129, v102
	v_cmp_ge_i32_e32 vcc, v148, v206
	s_waitcnt vmcnt(7)
	v_mfma_f32_16x16x32_f16 v[134:137], v[82:85], v[2:5], 0
	v_cndmask_b32_e32 v149, 3, v207, vcc
	v_mfma_f32_16x16x32_f16 v[138:141], v[82:85], v[34:37], 0
	v_mfma_f32_16x16x32_f16 v[142:145], v[82:85], v[30:33], 0
	v_mfma_f32_16x16x32_f16 v[150:153], v[82:85], v[26:29], 0
	v_mfma_f32_16x16x32_f16 v[154:157], v[82:85], v[22:25], 0
	v_mfma_f32_16x16x32_f16 v[130:133], v[82:85], v[18:21], 0
	v_mfma_f32_16x16x32_f16 v[118:121], v[82:85], v[14:17], 0
	v_mfma_f32_16x16x32_f16 v[98:101], v[82:85], v[10:13], 0
	v_mfma_f32_16x16x32_f16 v[38:41], v[82:85], v[6:9], 0
	s_waitcnt vmcnt(6)
	v_mfma_f32_16x16x32_f16 v[82:85], v[62:65], v[2:5], 0
	s_waitcnt vmcnt(5)
	v_mfma_f32_16x16x32_f16 v[86:89], v[58:61], v[2:5], 0
	s_waitcnt vmcnt(4)
	v_mfma_f32_16x16x32_f16 v[106:109], v[54:57], v[2:5], 0
	s_nop 0
	v_min3_i32 v50, v50, v51, v208
	v_min3_i32 v126, v52, v53, v50
	v_min3_i32 v46, v46, v47, v126
	v_min3_i32 v46, v48, v49, v46
	v_min3_i32 v42, v42, v43, v46
	v_min3_i32 v42, v44, v45, v42
	v_min3_i32 v42, v110, v111, v42
	v_min3_i32 v160, v112, v113, v42
	v_cmp_ge_i32_e32 vcc, v160, v208
	v_mfma_f32_16x16x32_f16 v[114:117], v[62:65], v[34:37], 0
	s_nop 0
	v_cndmask_b32_e32 v161, 3, v209, vcc
	v_mfma_f32_16x16x32_f16 v[122:125], v[58:61], v[34:37], 0
	v_mfma_f32_16x16x32_f16 v[90:93], v[54:57], v[34:37], 0
	s_nop 0
	v_min3_i32 v42, v134, v135, v182
	v_min3_i32 v42, v136, v137, v42
	v_min3_i32 v42, v82, v83, v42
	v_min3_i32 v42, v84, v85, v42
	v_min3_i32 v42, v86, v87, v42
	v_min3_i32 v42, v88, v89, v42
	v_min3_i32 v42, v106, v107, v42
	v_min3_i32 v134, v108, v109, v42
	v_cmp_ge_i32_e32 vcc, v134, v182
	v_mfma_f32_16x16x32_f16 v[94:97], v[62:65], v[30:33], 0
	s_nop 0
	v_cndmask_b32_e32 v135, 4, v183, vcc
	v_mfma_f32_16x16x32_f16 v[102:105], v[58:61], v[30:33], 0
	v_mfma_f32_16x16x32_f16 v[50:53], v[54:57], v[30:33], 0
	v_mfma_f32_16x16x32_f16 v[46:49], v[62:65], v[26:29], 0
	v_mfma_f32_16x16x32_f16 v[110:113], v[62:65], v[22:25], 0
	v_mfma_f32_16x16x32_f16 v[126:129], v[62:65], v[18:21], 0
	v_mfma_f32_16x16x32_f16 v[82:85], v[62:65], v[14:17], 0
	v_mfma_f32_16x16x32_f16 v[86:89], v[62:65], v[10:13], 0
	v_mfma_f32_16x16x32_f16 v[42:45], v[62:65], v[6:9], 0
	v_min3_i32 v62, v138, v139, v174
	v_min3_i32 v106, v140, v141, v62
	v_min3_i32 v106, v114, v115, v106
	v_min3_i32 v106, v116, v117, v106
	v_min3_i32 v114, v122, v123, v106
	v_min3_i32 v114, v124, v125, v114
	v_min3_i32 v90, v90, v91, v114
	v_min3_i32 v122, v92, v93, v90
	v_cmp_ge_i32_e32 vcc, v122, v174
	v_mfma_f32_16x16x32_f16 v[62:65], v[58:61], v[26:29], 0
	s_nop 0
	v_cndmask_b32_e32 v123, 4, v175, vcc
	v_mfma_f32_16x16x32_f16 v[106:109], v[54:57], v[26:29], 0
	s_nop 0
	v_min3_i32 v124, v142, v143, v176
	v_min3_i32 v124, v144, v145, v124
	v_min3_i32 v94, v94, v95, v124
	v_min3_i32 v124, v96, v97, v94
	v_min3_i32 v102, v102, v103, v124
	v_min3_i32 v102, v104, v105, v102
	v_min3_i32 v50, v50, v51, v102
	v_min3_i32 v124, v52, v53, v50
	v_cmp_ge_i32_e32 vcc, v124, v176
	v_mfma_f32_16x16x32_f16 v[90:93], v[58:61], v[22:25], 0
	s_nop 0
	v_cndmask_b32_e32 v125, 4, v177, vcc
	v_mfma_f32_16x16x32_f16 v[114:117], v[54:57], v[22:25], 0
	s_nop 0
	v_min3_i32 v136, v150, v151, v178
	v_min3_i32 v136, v152, v153, v136
	v_min3_i32 v46, v46, v47, v136
	v_min3_i32 v46, v48, v49, v46
	v_min3_i32 v62, v62, v63, v46
	v_min3_i32 v62, v64, v65, v62
	v_min3_i32 v62, v106, v107, v62
	v_min3_i32 v136, v108, v109, v62
	v_cmp_ge_i32_e32 vcc, v136, v178
	v_mfma_f32_16x16x32_f16 v[94:97], v[58:61], v[18:21], 0
	s_nop 0
	v_cndmask_b32_e32 v137, 4, v179, vcc
	v_mfma_f32_16x16x32_f16 v[46:49], v[54:57], v[18:21], 0
	s_nop 0
	v_min3_i32 v138, v154, v155, v166
	v_min3_i32 v138, v156, v157, v138
	v_min3_i32 v110, v110, v111, v138
	v_min3_i32 v110, v112, v113, v110
	v_min3_i32 v90, v90, v91, v110
	v_min3_i32 v90, v92, v93, v90
	v_min3_i32 v110, v114, v115, v90
	v_min3_i32 v138, v116, v117, v110
	v_cmp_ge_i32_e32 vcc, v138, v166
	v_mfma_f32_16x16x32_f16 v[102:105], v[58:61], v[14:17], 0
	v_mov_b32_e32 v154, 0
	v_cndmask_b32_e32 v139, 4, v167, vcc
	v_mfma_f32_16x16x32_f16 v[62:65], v[54:57], v[14:17], 0
	s_nop 0
	v_min3_i32 v114, v130, v131, v158
	v_min3_i32 v130, v132, v133, v114
	v_min3_i32 v126, v126, v127, v130
	v_min3_i32 v126, v128, v129, v126
	v_min3_i32 v94, v94, v95, v126
	v_min3_i32 v94, v96, v97, v94
	v_min3_i32 v46, v46, v47, v94
	v_min3_i32 v126, v48, v49, v46
	v_cmp_ge_i32_e32 vcc, v126, v158
	v_mfma_f32_16x16x32_f16 v[50:53], v[58:61], v[10:13], 0
	s_nop 0
	v_cndmask_b32_e32 v127, 4, v159, vcc
	v_mfma_f32_16x16x32_f16 v[106:109], v[54:57], v[10:13], 0
	s_nop 0
	v_min3_i32 v118, v118, v119, v146
	v_min3_i32 v118, v120, v121, v118
	v_min3_i32 v82, v82, v83, v118
	v_min3_i32 v118, v84, v85, v82
	v_min3_i32 v102, v102, v103, v118
	v_min3_i32 v102, v104, v105, v102
	v_min3_i32 v62, v62, v63, v102
	v_min3_i32 v102, v64, v65, v62
	v_cmp_ge_i32_e32 vcc, v102, v146
	v_mfma_f32_16x16x32_f16 v[58:61], v[58:61], v[6:9], 0
	v_and_b32_e32 v146, 7, v0
	v_cndmask_b32_e32 v103, 4, v147, vcc
	v_mfma_f32_16x16x32_f16 v[54:57], v[54:57], v[6:9], 0
	s_nop 0
	v_min3_i32 v98, v98, v99, v148
	v_min3_i32 v104, v100, v101, v98
	v_min3_i32 v86, v86, v87, v104
	v_min3_i32 v86, v88, v89, v86
	v_min3_i32 v50, v50, v51, v86
	v_min3_i32 v50, v52, v53, v50
	v_min3_i32 v50, v106, v107, v50
	v_min3_i32 v104, v108, v109, v50
	v_cmp_ge_i32_e32 vcc, v104, v148
	s_waitcnt vmcnt(3)
	v_mfma_f32_16x16x32_f16 v[90:93], v[78:81], v[2:5], 0
	v_cndmask_b32_e32 v105, 4, v149, vcc
	s_waitcnt vmcnt(2)
	v_mfma_f32_16x16x32_f16 v[110:113], v[74:77], v[2:5], 0
	s_waitcnt vmcnt(1)
	v_mfma_f32_16x16x32_f16 v[114:117], v[70:73], v[2:5], 0
	s_waitcnt vmcnt(0)
	v_mfma_f32_16x16x32_f16 v[2:5], v[66:69], v[2:5], 0
	s_nop 0
	v_min3_i32 v38, v38, v39, v160
	v_min3_i32 v38, v40, v41, v38
	v_min3_i32 v38, v42, v43, v38
	v_min3_i32 v42, v44, v45, v38
	v_min3_i32 v42, v58, v59, v42
	v_min3_i32 v42, v60, v61, v42
	v_min3_i32 v54, v54, v55, v42
	v_min3_i32 v106, v56, v57, v54
	v_cmp_ge_i32_e32 vcc, v106, v160
	v_mfma_f32_16x16x32_f16 v[46:49], v[78:81], v[34:37], 0
	s_nop 0
	v_cndmask_b32_e32 v107, 4, v161, vcc
	v_mfma_f32_16x16x32_f16 v[94:97], v[74:77], v[34:37], 0
	v_mfma_f32_16x16x32_f16 v[82:85], v[70:73], v[34:37], 0
	v_mfma_f32_16x16x32_f16 v[34:37], v[66:69], v[34:37], 0
	s_nop 0
	v_min3_i32 v54, v90, v91, v134
	v_min3_i32 v58, v92, v93, v54
	v_min3_i32 v58, v110, v111, v58
	v_min3_i32 v58, v112, v113, v58
	v_min3_i32 v90, v114, v115, v58
	v_min3_i32 v90, v116, v117, v90
	v_min3_i32 v2, v2, v3, v90
	v_min3_i32 v91, v4, v5, v2
	v_cmp_ge_i32_e32 vcc, v91, v134
	v_mfma_f32_16x16x32_f16 v[62:65], v[78:81], v[30:33], 0
	s_nop 0
	v_cndmask_b32_e32 v90, 5, v135, vcc
	v_add_u32_e32 v251, s3, v90
	v_lshl_or_b32 v90, v251, 2, v253
	ds_min_u64 v252, v[90:91] offset:16384
	v_mfma_f32_16x16x32_f16 v[98:101], v[74:77], v[30:33], 0
	v_mfma_f32_16x16x32_f16 v[86:89], v[70:73], v[30:33], 0
	v_mfma_f32_16x16x32_f16 v[30:33], v[66:69], v[30:33], 0
	s_nop 0
	v_min3_i32 v46, v46, v47, v122
	v_min3_i32 v46, v48, v49, v46
	v_min3_i32 v46, v94, v95, v46
	v_min3_i32 v92, v96, v97, v46
	v_min3_i32 v82, v82, v83, v92
	v_min3_i32 v82, v84, v85, v82
	v_min3_i32 v34, v34, v35, v82
	v_min3_i32 v93, v36, v37, v34
	v_cmp_ge_i32_e32 vcc, v93, v122
	v_mfma_f32_16x16x32_f16 v[50:53], v[78:81], v[26:29], 0
	s_nop 0
	v_cndmask_b32_e32 v92, 5, v123, vcc
	v_add_u32_e32 v251, s3, v92
	v_lshl_or_b32 v92, v251, 2, v253
	ds_min_u64 v252, v[92:93] offset:16512
	v_mfma_f32_16x16x32_f16 v[38:41], v[74:77], v[26:29], 0
	v_mfma_f32_16x16x32_f16 v[42:45], v[70:73], v[26:29], 0
	v_mfma_f32_16x16x32_f16 v[26:29], v[66:69], v[26:29], 0
	s_nop 0
	v_min3_i32 v62, v62, v63, v124
	v_min3_i32 v62, v64, v65, v62
	v_min3_i32 v62, v98, v99, v62
	v_min3_i32 v62, v100, v101, v62
	v_min3_i32 v86, v86, v87, v62
	v_min3_i32 v86, v88, v89, v86
	v_min3_i32 v30, v30, v31, v86
	v_min3_i32 v95, v32, v33, v30
	v_cmp_ge_i32_e32 vcc, v95, v124
	v_mfma_f32_16x16x32_f16 v[54:57], v[78:81], v[22:25], 0
	s_nop 0
	v_cndmask_b32_e32 v94, 5, v125, vcc
	v_add_u32_e32 v251, s3, v94
	v_lshl_or_b32 v94, v251, 2, v253
	ds_min_u64 v252, v[94:95] offset:16640
	v_mfma_f32_16x16x32_f16 v[58:61], v[74:77], v[22:25], 0
	v_mfma_f32_16x16x32_f16 v[2:5], v[70:73], v[22:25], 0
	v_mfma_f32_16x16x32_f16 v[22:25], v[66:69], v[22:25], 0
	s_nop 0
	v_min3_i32 v50, v50, v51, v136
	v_min3_i32 v50, v52, v53, v50
	v_min3_i32 v38, v38, v39, v50
	v_min3_i32 v38, v40, v41, v38
	v_min3_i32 v38, v42, v43, v38
	v_min3_i32 v38, v44, v45, v38
	v_min3_i32 v26, v26, v27, v38
	v_min3_i32 v51, v28, v29, v26
	v_cmp_ge_i32_e32 vcc, v51, v136
	v_mfma_f32_16x16x32_f16 v[46:49], v[78:81], v[18:21], 0
	s_nop 0
	v_cndmask_b32_e32 v50, 5, v137, vcc
	v_add_u32_e32 v251, s3, v50
	v_lshl_or_b32 v50, v251, 2, v253
	ds_min_u64 v252, v[50:51] offset:16768
	v_mfma_f32_16x16x32_f16 v[82:85], v[74:77], v[18:21], 0
	v_mfma_f32_16x16x32_f16 v[34:37], v[70:73], v[18:21], 0
	v_mfma_f32_16x16x32_f16 v[18:21], v[66:69], v[18:21], 0
	s_nop 0
	v_min3_i32 v42, v54, v55, v138
	v_min3_i32 v52, v56, v57, v42
	v_min3_i32 v52, v58, v59, v52
	v_min3_i32 v52, v60, v61, v52
	v_min3_i32 v2, v2, v3, v52
	v_min3_i32 v2, v4, v5, v2
	v_min3_i32 v2, v22, v23, v2
	v_min3_i32 v53, v24, v25, v2
	v_cmp_ge_i32_e32 vcc, v53, v138
	v_mfma_f32_16x16x32_f16 v[62:65], v[78:81], v[14:17], 0
	s_nop 0
	v_cndmask_b32_e32 v52, 5, v139, vcc
	v_add_u32_e32 v251, s3, v52
	v_lshl_or_b32 v52, v251, 2, v253
	ds_min_u64 v252, v[52:53] offset:16896
	v_mfma_f32_16x16x32_f16 v[30:33], v[74:77], v[14:17], 0
	v_mfma_f32_16x16x32_f16 v[86:89], v[70:73], v[14:17], 0
	v_mfma_f32_16x16x32_f16 v[14:17], v[66:69], v[14:17], 0
	s_nop 0
	v_min3_i32 v46, v46, v47, v126
	v_min3_i32 v46, v48, v49, v46
	v_min3_i32 v54, v82, v83, v46
	v_min3_i32 v54, v84, v85, v54
	v_min3_i32 v34, v34, v35, v54
	v_min3_i32 v34, v36, v37, v34
	v_min3_i32 v18, v18, v19, v34
	v_min3_i32 v19, v20, v21, v18
	v_cmp_ge_i32_e32 vcc, v19, v126
	v_mfma_f32_16x16x32_f16 v[38:41], v[78:81], v[10:13], 0
	s_nop 0
	v_cndmask_b32_e32 v18, 5, v127, vcc
	v_add_u32_e32 v251, s3, v18
	v_lshl_or_b32 v18, v251, 2, v253
	ds_min_u64 v252, v[18:19] offset:17024
	v_mfma_f32_16x16x32_f16 v[26:29], v[74:77], v[10:13], 0
	v_mfma_f32_16x16x32_f16 v[42:45], v[70:73], v[10:13], 0
	v_mfma_f32_16x16x32_f16 v[10:13], v[66:69], v[10:13], 0
	s_nop 0
	v_min3_i32 v20, v62, v63, v102
	v_min3_i32 v20, v64, v65, v20
	v_min3_i32 v20, v30, v31, v20
	v_min3_i32 v20, v32, v33, v20
	v_min3_i32 v20, v86, v87, v20
	v_min3_i32 v20, v88, v89, v20
	v_min3_i32 v14, v14, v15, v20
	v_min3_i32 v15, v16, v17, v14
	v_cmp_ge_i32_e32 vcc, v15, v102
	v_mfma_f32_16x16x32_f16 v[2:5], v[78:81], v[6:9], 0
	v_bfe_u32 v17, v0, 4, 2
	v_cndmask_b32_e32 v14, 5, v103, vcc
	v_add_u32_e32 v251, s3, v14
	v_lshl_or_b32 v14, v251, 2, v253
	ds_min_u64 v252, v[14:15] offset:17152
	v_mfma_f32_16x16x32_f16 v[22:25], v[74:77], v[6:9], 0
	v_mfma_f32_16x16x32_f16 v[46:49], v[70:73], v[6:9], 0
	v_mfma_f32_16x16x32_f16 v[6:9], v[66:69], v[6:9], 0
	s_nop 0
	v_min3_i32 v16, v38, v39, v104
	v_min3_i32 v16, v40, v41, v16
	v_min3_i32 v16, v26, v27, v16
	v_min3_i32 v2, v2, v3, v106
	v_min3_i32 v16, v28, v29, v16
	v_min3_i32 v2, v4, v5, v2
	v_min3_i32 v16, v42, v43, v16
	v_min3_i32 v2, v22, v23, v2
	v_lshlrev_b32_e32 v4, 3, v210
	v_min3_i32 v16, v44, v45, v16
	v_min3_i32 v2, v24, v25, v2
	v_min3_i32 v10, v10, v11, v16
	v_min3_i32 v2, v46, v47, v2
	v_min3_i32 v11, v12, v13, v10
	v_min3_i32 v2, v48, v49, v2
	v_cmp_ge_i32_e32 vcc, v11, v104
	v_min3_i32 v2, v6, v7, v2
	v_cndmask_b32_e32 v10, 5, v105, vcc
	v_add_u32_e32 v251, s3, v10
	v_lshl_or_b32 v10, v251, 2, v253
	ds_min_u64 v252, v[10:11] offset:17280
	v_min3_i32 v3, v8, v9, v2
	v_cmp_ge_i32_e32 vcc, v3, v106
	v_cndmask_b32_e32 v2, 5, v107, vcc
	v_add_u32_e32 v2, s3, v2
	v_bfe_u32 v10, v0, 3, 3
	s_lshl_b32 s3, s15, 3
	v_lshl_or_b32 v2, v2, 2, v17
	v_or_b32_e32 v151, s3, v10
	ds_min_u64 v4, v[2:3] offset:17408
	v_lshlrev_b32_e32 v2, 3, v151
	s_waitcnt lgkmcnt(0)
	s_barrier
	ds_read2st64_b32 v[4:5], v2 offset0:64 offset1:66
	s_add_i32 s2, s3, s11
	s_lshr_b32 s2, s2, 4
	s_add_i32 s2, s2, s8
	s_waitcnt lgkmcnt(0)
	v_ashrrev_i32_e32 v3, 2, v4
	v_mul_hi_i32 v6, v3, s12
	v_lshrrev_b32_e32 v7, 31, v6
	v_add_u32_e32 v6, v6, v7
	v_mul_lo_u32 v7, v6, -6
	v_mul_lo_u32 v6, v6, 24
	v_min_i32_e32 v6, 0xa5, v6
	v_add_lshl_u32 v7, v7, v3, 2
	v_bfe_u32 v3, v0, 2, 1
	v_add3_u32 v152, v6, v3, v7
	v_lshlrev_b32_e32 v6, 2, v4
	v_and_b32_e32 v4, 3, v0
	v_and_or_b32 v153, v6, 12, v4
	v_add_u32_e32 v6, s9, v152
	v_lshl_or_b32 v6, v6, 6, v153
	v_bitop3_b32 v7, s3, 15, v10 bitop3:0xc8
	v_lshl_or_b32 v7, v4, 4, v7
	v_lshl_or_b32 v8, s2, 6, v7
	v_ashrrev_i32_e32 v7, 31, v6
	v_lshl_add_u64 v[6:7], v[6:7], 4, s[6:7]
	v_ashrrev_i32_e32 v9, 31, v8
	v_lshl_add_u64 v[8:9], v[8:9], 4, s[4:5]
	global_load_dwordx4 v[126:129], v[6:7], off
	global_load_dwordx4 v[114:117], v[6:7], off offset:256
	global_load_dwordx4 v[130:133], v[6:7], off offset:2048
	global_load_dwordx4 v[118:121], v[6:7], off offset:2304
	global_load_dwordx4 v[134:137], v[8:9], off
	global_load_dwordx4 v[102:105], v[6:7], off offset:512
	global_load_dwordx4 v[78:81], v[6:7], off offset:768
	global_load_dwordx4 v[106:109], v[6:7], off offset:2560
	global_load_dwordx4 v[82:85], v[6:7], off offset:2816
	v_ashrrev_i32_e32 v6, 2, v5
	v_mul_hi_i32 v7, v6, s12
	v_lshrrev_b32_e32 v11, 31, v7
	v_add_u32_e32 v7, v7, v11
	v_mul_lo_u32 v11, v7, -6
	v_mul_lo_u32 v7, v7, 24
	s_add_i32 s2, s3, 64
	v_min_i32_e32 v7, 0xa5, v7
	v_add_lshl_u32 v6, v11, v6, 2
	s_add_i32 s3, s2, s11
	v_add3_u32 v148, v7, v3, v6
	v_lshlrev_b32_e32 v5, 2, v5
	v_and_or_b32 v149, v5, 12, v4
	v_add_u32_e32 v5, s9, v148
	s_lshr_b32 s3, s3, 4
	v_lshl_or_b32 v6, v5, 6, v149
	s_add_i32 s3, s3, s8
	v_bitop3_b32 v5, s2, 15, v10 bitop3:0xc8
	v_lshl_or_b32 v5, v4, 4, v5
	v_lshl_or_b32 v10, s3, 6, v5
	v_ashrrev_i32_e32 v7, 31, v6
	v_ashrrev_i32_e32 v11, 31, v10
	v_lshl_add_u64 v[6:7], v[6:7], 4, s[6:7]
	v_lshl_add_u64 v[10:11], v[10:11], 4, s[4:5]
	global_load_dwordx4 v[110:113], v[10:11], off
	global_load_dwordx4 v[90:93], v[6:7], off
	global_load_dwordx4 v[62:65], v[6:7], off offset:256
	global_load_dwordx4 v[94:97], v[6:7], off offset:2048
	global_load_dwordx4 v[66:69], v[6:7], off offset:2304
	global_load_dwordx4 v[38:41], v[6:7], off offset:512
	global_load_dwordx4 v[18:21], v[6:7], off offset:768
	global_load_dwordx4 v[42:45], v[6:7], off offset:2560
	global_load_dwordx4 v[22:25], v[6:7], off offset:2816
	s_cmpk_lt_u32 s10, 0x80
	s_cselect_b64 s[2:3], -1, 0
	s_cmpk_gt_u32 s10, 0x7f
	s_cbranch_scc1 .LBB1_4
	v_add_u32_e32 v2, 0x4000, v2
	ds_read_b32 v2, v2 offset:1024
	v_or_b32_e32 v147, 0x80, v151
	v_add_u32_e32 v5, s11, v147
	s_waitcnt lgkmcnt(0)
	v_ashrrev_i32_e32 v6, 2, v2
	v_mul_hi_i32 v7, v6, s12
	v_lshrrev_b32_e32 v8, 31, v7
	v_add_u32_e32 v7, v7, v8
	v_mul_lo_u32 v8, v7, -6
	v_mul_lo_u32 v7, v7, 24
	v_min_i32_e32 v7, 0xa5, v7
	v_add_lshl_u32 v6, v8, v6, 2
	v_add3_u32 v150, v7, v3, v6
	v_lshlrev_b32_e32 v2, 2, v2
	v_lshrrev_b32_e32 v3, 4, v5
	v_and_or_b32 v155, v2, 12, v4
	v_add_u32_e32 v2, s9, v150
	v_add_u32_e32 v3, s8, v3
	v_lshl_or_b32 v2, v2, 6, v155
	v_lshl_or_b32 v4, v4, 4, v151
	v_lshl_or_b32 v4, v3, 6, v4
	v_ashrrev_i32_e32 v3, 31, v2
	v_ashrrev_i32_e32 v5, 31, v4
	v_lshl_add_u64 v[2:3], v[2:3], 4, s[6:7]
	v_lshl_add_u64 v[50:51], v[4:5], 4, s[4:5]
	global_load_dwordx4 v[58:61], v[2:3], off
	global_load_dwordx4 v[46:49], v[2:3], off offset:256
	global_load_dwordx4 v[34:37], v[2:3], off offset:2048
	global_load_dwordx4 v[10:13], v[2:3], off offset:2304
	global_load_dwordx4 v[98:101], v[50:51], off
	global_load_dwordx4 v[30:33], v[2:3], off offset:512
	global_load_dwordx4 v[14:17], v[2:3], off offset:768
	global_load_dwordx4 v[6:9], v[2:3], off offset:2560
	s_nop 0
	global_load_dwordx4 v[2:5], v[2:3], off offset:2816
	s_nop 0
	s_nop 0
	v_lshl_or_b32 v150, v150, 4, v155
	s_branch .LBB1_5
